# merge context-row tiles: all fragment loads of both products issued ahead, LDS partial reads batched
# speedup vs baseline: 1.0077x; 1.0077x over previous
; __device__ __forceinline__ unsigned pk2(float lo, float hi) { f32x2 v = {lo, hi}; return __builtin_bit_cast(unsigned, __builtin_convertvector(v, bf2_t)); }
; __device__ __forceinline__ float bflo(unsigned u) { return __uint_as_float(u << 16); }
; __device__ __forceinline__ float bfhi(unsigned u) { return __uint_as_float(u & 0xffff0000u); }
; template <int NS  > __device__ __forceinline__ f32x4 ctx_tile(Frame& F, const bf16* A, const bf16* Bt, int r0, int c0) {
;     ...
;     const bf16* ap = A + (size_t)(r0 + l15) * K + w * (K / 8) + 8 * g;
;     const bf16* bp = Bt + (size_t)(c0 + l15) * K + w * (K / 8) + 8 * g;
;     f32x4 acc[4][2];
; #pragma unroll
;     for (int rt = 0; rt < 4; ++rt) { acc[rt][0] = (f32x4){0.f, 0.f, 0.f, 0.f}; acc[rt][1] = (f32x4){0.f, 0.f, 0.f, 0.f}; }
; #pragma unroll 4
;     for (int s = 0; s < NS; ++s) {
;         bf16x8 af[4], bf[2];
; #pragma unroll
;         for (int rt = 0; rt < 4; ++rt) af[rt] = *(const bf16x8*)(ap + (size_t)(16 * rt) * K + 32 * s);
;         bf[0] = *(const bf16x8*)(bp + 32 * s); bf[1] = *(const bf16x8*)(bp + (size_t)16 * K + 32 * s);
; #pragma unroll
;         for (int rt = 0; rt < 4; ++rt) { acc[rt][0] = __builtin_amdgcn_mfma_f32_16x16x32_bf16(bf[0], af[rt], acc[rt][0], 0, 0, 0); acc[rt][1] = __builtin_amdgcn_mfma_f32_16x16x32_bf16(bf[1], af[rt], acc[rt][1], 0, 0, 0); }
;     }
; __global__ void __launch_bounds__(NWAVES * 64, 2) mk_fwd(Args args) {
;     ...
;             if (!last) for (int tl = F.vcu; tl < 256; tl += F.G) {
;                 const int r0 = ML + 64 * (tl >> 5), c0 = 32 * (tl & 31);
;                 const int tt = F.tid >> 6; const size_t row = (size_t)(r0 + 16 * (tt >> 1) + (F.lane & 15)); const int col = c0 + 16 * (tt & 1) + 4 * (F.lane >> 4);
;                 const u32x2 ga = *(const u32x2*)((const bf16*)(ws + WS_P) + row * INC + OFF_GA + col), gr = *(const u32x2*)((const bf16*)(ws + WS_P) + row * INC + OFF_GR + col);
;                 const f32x4 s1 = ctx_tile<4>(F, (const bf16*)(ws + WS_ATT), WO, r0, c0);
;                 const f32x4 s2 = ctx_tile<4>(F, (const bf16*)(ws + WS_RECG), WO + (size_t)D * D, r0, c0);
;                 u32x2 o2; o2.x = pk2(bflo(ga.x) * s1[0] + bflo(gr.x) * s2[0], bfhi(ga.x) * s1[1] + bfhi(gr.x) * s2[1]); o2.y = pk2(bflo(ga.y) * s1[2] + bflo(gr.y) * s2[2], bfhi(ga.y) * s1[3] + bfhi(gr.y) * s2[3]);
.LBB13_853:
	s_and_b32 s4, s0, 0xffffffc0
	s_add_i32 s8, s4, 0x4000
	s_and_b32 s9, s2, 0x3e0
	v_add_u32_e32 v10, s8, v35
	v_or_b32_e32 v12, s9, v36
	v_mad_i64_i32 v[14:15], s[4:5], v10, s91, v[132:133]
	v_lshlrev_b32_e32 v12, 1, v12
	v_mov_b32_e32 v13, v98
	v_lshl_add_u64 v[16:17], v[14:15], 0, v[12:13]
	v_add_co_u32_e32 v14, vcc, 0x1000, v16
	v_or_b32_e32 v18, s8, v34
	s_nop 0
	v_addc_co_u32_e32 v15, vcc, 0, v17, vcc
	v_ashrrev_i32_e32 v19, 31, v18
	v_add_co_u32_e32 v16, vcc, 0x2000, v16
	v_lshlrev_b64 v[24:25], 11, v[18:19]
	s_nop 0
	v_addc_co_u32_e32 v17, vcc, 0, v17, vcc
	global_load_dwordx2 v[14:15], v[14:15], off offset:3072
	global_load_dwordx2 v[16:17], v[16:17], off offset:1024
	v_lshl_add_u64 v[136:137], v[2:3], 0, v[24:25]
	v_add_co_u32_e32 v138, vcc, 0x8000, v136
	s_nop 1
	v_addc_co_u32_e32 v139, vcc, 0, v137, vcc
	v_add_co_u32_e32 v140, vcc, s57, v136
	s_nop 1
	v_addc_co_u32_e32 v141, vcc, 0, v137, vcc
	v_add_co_u32_e32 v142, vcc, s64, v136
	s_nop 1
	v_addc_co_u32_e32 v143, vcc, 0, v137, vcc
	v_lshl_add_u64 v[148:149], v[6:7], 0, v[24:25]
	v_add_co_u32_e32 v150, vcc, 0x8000, v148
	s_nop 1
	v_addc_co_u32_e32 v151, vcc, 0, v149, vcc
	v_add_co_u32_e32 v152, vcc, s57, v148
	s_nop 1
	v_addc_co_u32_e32 v153, vcc, 0, v149, vcc
	v_add_co_u32_e32 v154, vcc, s64, v148
	s_nop 1
	v_addc_co_u32_e32 v155, vcc, 0, v149, vcc
	v_or_b32_e32 v18, s9, v34
	v_lshlrev_b32_e32 v18, 11, v18
	v_mov_b32_e32 v19, v98
	v_lshl_add_u64 v[144:145], v[4:5], 0, v[18:19]
	v_add_co_u32_e32 v146, vcc, 0x8000, v144
	s_nop 1
	v_addc_co_u32_e32 v147, vcc, 0, v145, vcc
	v_lshl_add_u64 v[156:157], v[8:9], 0, v[18:19]
	v_add_co_u32_e32 v158, vcc, 0x8000, v156
	s_nop 1
	v_addc_co_u32_e32 v159, vcc, 0, v157, vcc
	v_ashrrev_i32_e32 v11, 31, v10
	v_lshlrev_b64 v[10:11], 11, v[10:11]
	v_lshl_add_u64 v[10:11], s[6:7], 0, v[10:11]
	v_lshl_add_u64 v[10:11], v[10:11], 0, v[12:13]
	global_load_dwordx4 v[38:41], v[136:137], off
	global_load_dwordx4 v[42:45], v[138:139], off
	global_load_dwordx4 v[46:49], v[140:141], off
	global_load_dwordx4 v[50:53], v[142:143], off
	global_load_dwordx4 v[54:57], v[144:145], off
	global_load_dwordx4 v[58:61], v[146:147], off
	global_load_dwordx4 v[62:65], v[136:137], off offset:64
	global_load_dwordx4 v[66:69], v[138:139], off offset:64
	global_load_dwordx4 v[70:73], v[140:141], off offset:64
	global_load_dwordx4 v[74:77], v[142:143], off offset:64
	global_load_dwordx4 v[78:81], v[144:145], off offset:64
	global_load_dwordx4 v[82:85], v[146:147], off offset:64
	global_load_dwordx4 v[86:89], v[136:137], off offset:128
	global_load_dwordx4 v[90:93], v[138:139], off offset:128
	global_load_dwordx4 v[94:97], v[140:141], off offset:128
	global_load_dwordx4 v[208:211], v[142:143], off offset:128
	global_load_dwordx4 v[212:215], v[144:145], off offset:128
	global_load_dwordx4 v[216:219], v[146:147], off offset:128
	global_load_dwordx4 v[220:223], v[136:137], off offset:192
	global_load_dwordx4 v[224:227], v[138:139], off offset:192
	global_load_dwordx4 v[228:231], v[140:141], off offset:192
	global_load_dwordx4 v[242:245], v[142:143], off offset:192
	global_load_dwordx4 v[160:163], v[144:145], off offset:192
	global_load_dwordx4 v[30:33], v[146:147], off offset:192
	s_waitcnt vmcnt(18)
	v_mfma_f32_16x16x32_bf16 v[100:103], v[54:57], v[38:41], 0
	v_mfma_f32_16x16x32_bf16 v[104:107], v[58:61], v[38:41], 0
	v_mfma_f32_16x16x32_bf16 v[108:111], v[54:57], v[42:45], 0
	v_mfma_f32_16x16x32_bf16 v[112:115], v[58:61], v[42:45], 0
	v_mfma_f32_16x16x32_bf16 v[116:119], v[54:57], v[46:49], 0
	v_mfma_f32_16x16x32_bf16 v[120:123], v[58:61], v[46:49], 0
	v_mfma_f32_16x16x32_bf16 v[124:127], v[54:57], v[50:53], 0
	v_mfma_f32_16x16x32_bf16 v[128:131], v[58:61], v[50:53], 0
	global_load_dwordx4 v[38:41], v[148:149], off
	global_load_dwordx4 v[42:45], v[150:151], off
	global_load_dwordx4 v[46:49], v[152:153], off
	global_load_dwordx4 v[50:53], v[154:155], off
	global_load_dwordx4 v[54:57], v[156:157], off
	global_load_dwordx4 v[58:61], v[158:159], off
	s_waitcnt vmcnt(18)
	v_mfma_f32_16x16x32_bf16 v[100:103], v[78:81], v[62:65], v[100:103]
	v_mfma_f32_16x16x32_bf16 v[104:107], v[82:85], v[62:65], v[104:107]
	v_mfma_f32_16x16x32_bf16 v[108:111], v[78:81], v[66:69], v[108:111]
	v_mfma_f32_16x16x32_bf16 v[112:115], v[82:85], v[66:69], v[112:115]
	v_mfma_f32_16x16x32_bf16 v[116:119], v[78:81], v[70:73], v[116:119]
	v_mfma_f32_16x16x32_bf16 v[120:123], v[82:85], v[70:73], v[120:123]
	v_mfma_f32_16x16x32_bf16 v[124:127], v[78:81], v[74:77], v[124:127]
	v_mfma_f32_16x16x32_bf16 v[128:131], v[82:85], v[74:77], v[128:131]
	global_load_dwordx4 v[62:65], v[148:149], off offset:64
	global_load_dwordx4 v[66:69], v[150:151], off offset:64
	global_load_dwordx4 v[70:73], v[152:153], off offset:64
	global_load_dwordx4 v[74:77], v[154:155], off offset:64
	global_load_dwordx4 v[78:81], v[156:157], off offset:64
	global_load_dwordx4 v[82:85], v[158:159], off offset:64
	s_waitcnt vmcnt(18)
	v_mfma_f32_16x16x32_bf16 v[100:103], v[212:215], v[86:89], v[100:103]
	v_mfma_f32_16x16x32_bf16 v[104:107], v[216:219], v[86:89], v[104:107]
	v_mfma_f32_16x16x32_bf16 v[108:111], v[212:215], v[90:93], v[108:111]
	v_mfma_f32_16x16x32_bf16 v[112:115], v[216:219], v[90:93], v[112:115]
	v_mfma_f32_16x16x32_bf16 v[116:119], v[212:215], v[94:97], v[116:119]
	v_mfma_f32_16x16x32_bf16 v[120:123], v[216:219], v[94:97], v[120:123]
	v_mfma_f32_16x16x32_bf16 v[124:127], v[212:215], v[208:211], v[124:127]
	v_mfma_f32_16x16x32_bf16 v[128:131], v[216:219], v[208:211], v[128:131]
	global_load_dwordx4 v[86:89], v[148:149], off offset:128
	global_load_dwordx4 v[90:93], v[150:151], off offset:128
	global_load_dwordx4 v[94:97], v[152:153], off offset:128
	global_load_dwordx4 v[208:211], v[154:155], off offset:128
	global_load_dwordx4 v[212:215], v[156:157], off offset:128
	global_load_dwordx4 v[216:219], v[158:159], off offset:128
	s_waitcnt vmcnt(18)
	v_mfma_f32_16x16x32_bf16 v[100:103], v[160:163], v[220:223], v[100:103]
	v_mfma_f32_16x16x32_bf16 v[104:107], v[30:33], v[220:223], v[104:107]
	v_mfma_f32_16x16x32_bf16 v[108:111], v[160:163], v[224:227], v[108:111]
	v_mfma_f32_16x16x32_bf16 v[112:115], v[30:33], v[224:227], v[112:115]
	v_mfma_f32_16x16x32_bf16 v[116:119], v[160:163], v[228:231], v[116:119]
	v_mfma_f32_16x16x32_bf16 v[120:123], v[30:33], v[228:231], v[120:123]
	v_mfma_f32_16x16x32_bf16 v[124:127], v[160:163], v[242:245], v[124:127]
	v_mfma_f32_16x16x32_bf16 v[128:131], v[30:33], v[242:245], v[128:131]
	global_load_dwordx4 v[220:223], v[148:149], off offset:192
	global_load_dwordx4 v[224:227], v[150:151], off offset:192
	global_load_dwordx4 v[228:231], v[152:153], off offset:192
	global_load_dwordx4 v[242:245], v[154:155], off offset:192
	global_load_dwordx4 v[160:163], v[156:157], off offset:192
	global_load_dwordx4 v[30:33], v[158:159], off offset:192
	s_barrier
; #define LAS __attribute__((address_space(3)))
; __device__ __forceinline__ unsigned pk2(float lo, float hi) { f32x2 v = {lo, hi}; return __builtin_bit_cast(unsigned, __builtin_convertvector(v, bf2_t)); }
; __device__ __forceinline__ float bflo(unsigned u) { return __uint_as_float(u << 16); }
; __device__ __forceinline__ float bfhi(unsigned u) { return __uint_as_float(u & 0xffff0000u); }
; template <int NS  > __device__ __forceinline__ f32x4 ctx_tile(Frame& F, const bf16* A, const bf16* Bt, int r0, int c0) {
;     ...
;     LAS f32x4* red = (LAS f32x4*)F.lds;
;     __syncthreads();
; #pragma unroll
;     for (int rt = 0; rt < 4; ++rt) { red[(w * 8 + 2 * rt) * 64 + lane] = acc[rt][0]; red[(w * 8 + 2 * rt + 1) * 64 + lane] = acc[rt][1]; }
;     __syncthreads();
;     const int tt = F.tid >> 6;
;     f32x4 v = red[tt * 64 + lane];
; #pragma unroll
;     for (int ww = 1; ww < 8; ++ww) v = v + red[(ww * 8 + tt) * 64 + lane];
;     return v;
; __global__ void __launch_bounds__(NWAVES * 64, 2) mk_fwd(Args args) {
;     ...
;                 const f32x4 s1 = ctx_tile<4>(F, (const bf16*)(ws + WS_ATT), WO, r0, c0);
;                 const f32x4 s2 = ctx_tile<4>(F, (const bf16*)(ws + WS_RECG), WO + (size_t)D * D, r0, c0);
;                 u32x2 o2; o2.x = pk2(bflo(ga.x) * s1[0] + bflo(gr.x) * s2[0], bfhi(ga.x) * s1[1] + bfhi(gr.x) * s2[1]); o2.y = pk2(bflo(ga.y) * s1[2] + bflo(gr.y) * s2[2], bfhi(ga.y) * s1[3] + bfhi(gr.y) * s2[3]);
;                 *(u32x2*)((bf16*)(ws + WS_MM) + row * D + col) = o2;
	s_nop 7
	ds_write_b128 v37, v[100:103]
	ds_write_b128 v37, v[104:107] offset:1024
	ds_write_b128 v37, v[108:111] offset:2048
	ds_write_b128 v37, v[112:115] offset:3072
	ds_write_b128 v37, v[116:119] offset:4096
	ds_write_b128 v37, v[120:123] offset:5120
	ds_write_b128 v37, v[124:127] offset:6144
	ds_write_b128 v37, v[128:131] offset:7168
	s_waitcnt lgkmcnt(0)
	s_barrier
	ds_read_b128 v[100:103], v1
	ds_read_b128 v[104:107], v1 offset:8192
	ds_read_b128 v[108:111], v1 offset:16384
	ds_read_b128 v[112:115], v1 offset:24576
	ds_read_b128 v[116:119], v1 offset:32768
	ds_read_b128 v[120:123], v1 offset:40960
	ds_read_b128 v[124:127], v1 offset:49152
	ds_read_b128 v[128:131], v1 offset:57344
	s_waitcnt lgkmcnt(6)
	v_pk_add_f32 v[232:233], v[102:103], v[106:107]
	v_pk_add_f32 v[198:199], v[100:101], v[104:105]
	s_waitcnt lgkmcnt(5)
	v_pk_add_f32 v[232:233], v[232:233], v[110:111]
	v_pk_add_f32 v[198:199], v[198:199], v[108:109]
	s_waitcnt lgkmcnt(4)
	v_pk_add_f32 v[232:233], v[232:233], v[114:115]
	v_pk_add_f32 v[198:199], v[198:199], v[112:113]
	s_waitcnt lgkmcnt(3)
	v_pk_add_f32 v[232:233], v[232:233], v[118:119]
	v_pk_add_f32 v[198:199], v[198:199], v[116:117]
	s_waitcnt lgkmcnt(2)
	v_pk_add_f32 v[232:233], v[232:233], v[122:123]
	v_pk_add_f32 v[198:199], v[198:199], v[120:121]
	s_waitcnt lgkmcnt(1)
	v_pk_add_f32 v[232:233], v[232:233], v[126:127]
	v_pk_add_f32 v[198:199], v[198:199], v[124:125]
	s_waitcnt lgkmcnt(0)
	v_pk_add_f32 v[232:233], v[232:233], v[130:131]
	v_pk_add_f32 v[198:199], v[198:199], v[128:129]
	s_waitcnt vmcnt(18)
	v_mfma_f32_16x16x32_bf16 v[166:169], v[54:57], v[38:41], 0
	v_mfma_f32_16x16x32_bf16 v[170:173], v[58:61], v[38:41], 0
	v_mfma_f32_16x16x32_bf16 v[174:177], v[54:57], v[42:45], 0
	v_mfma_f32_16x16x32_bf16 v[178:181], v[58:61], v[42:45], 0
	v_mfma_f32_16x16x32_bf16 v[182:185], v[54:57], v[46:49], 0
	v_mfma_f32_16x16x32_bf16 v[186:189], v[58:61], v[46:49], 0
	v_mfma_f32_16x16x32_bf16 v[190:193], v[54:57], v[50:53], 0
	v_mfma_f32_16x16x32_bf16 v[194:197], v[58:61], v[50:53], 0
	s_waitcnt vmcnt(12)
	v_mfma_f32_16x16x32_bf16 v[166:169], v[78:81], v[62:65], v[166:169]
	v_mfma_f32_16x16x32_bf16 v[170:173], v[82:85], v[62:65], v[170:173]
	v_mfma_f32_16x16x32_bf16 v[174:177], v[78:81], v[66:69], v[174:177]
	v_mfma_f32_16x16x32_bf16 v[178:181], v[82:85], v[66:69], v[178:181]
	v_mfma_f32_16x16x32_bf16 v[182:185], v[78:81], v[70:73], v[182:185]
	v_mfma_f32_16x16x32_bf16 v[186:189], v[82:85], v[70:73], v[186:189]
	v_mfma_f32_16x16x32_bf16 v[190:193], v[78:81], v[74:77], v[190:193]
	v_mfma_f32_16x16x32_bf16 v[194:197], v[82:85], v[74:77], v[194:197]
	s_waitcnt vmcnt(6)
	v_mfma_f32_16x16x32_bf16 v[166:169], v[212:215], v[86:89], v[166:169]
	v_mfma_f32_16x16x32_bf16 v[170:173], v[216:219], v[86:89], v[170:173]
	v_mfma_f32_16x16x32_bf16 v[174:177], v[212:215], v[90:93], v[174:177]
	v_mfma_f32_16x16x32_bf16 v[178:181], v[216:219], v[90:93], v[178:181]
	v_mfma_f32_16x16x32_bf16 v[182:185], v[212:215], v[94:97], v[182:185]
	v_mfma_f32_16x16x32_bf16 v[186:189], v[216:219], v[94:97], v[186:189]
	v_mfma_f32_16x16x32_bf16 v[190:193], v[212:215], v[208:211], v[190:193]
	v_mfma_f32_16x16x32_bf16 v[194:197], v[216:219], v[208:211], v[194:197]
	s_waitcnt vmcnt(0)
	v_mfma_f32_16x16x32_bf16 v[166:169], v[160:163], v[220:223], v[166:169]
	v_mfma_f32_16x16x32_bf16 v[170:173], v[30:33], v[220:223], v[170:173]
	v_mfma_f32_16x16x32_bf16 v[174:177], v[160:163], v[224:227], v[174:177]
	v_mfma_f32_16x16x32_bf16 v[178:181], v[30:33], v[224:227], v[178:181]
	v_mfma_f32_16x16x32_bf16 v[182:185], v[160:163], v[228:231], v[182:185]
	v_mfma_f32_16x16x32_bf16 v[186:189], v[30:33], v[228:231], v[186:189]
	v_mfma_f32_16x16x32_bf16 v[190:193], v[160:163], v[242:245], v[190:193]
	v_mfma_f32_16x16x32_bf16 v[194:197], v[30:33], v[242:245], v[194:197]
	s_barrier
	s_nop 7
	ds_write_b128 v37, v[166:169]
	ds_write_b128 v37, v[170:173] offset:1024
	ds_write_b128 v37, v[174:177] offset:2048
	ds_write_b128 v37, v[178:181] offset:3072
	ds_write_b128 v37, v[182:185] offset:4096
	ds_write_b128 v37, v[186:189] offset:5120
	ds_write_b128 v37, v[190:193] offset:6144
	ds_write_b128 v37, v[194:197] offset:7168
	s_waitcnt lgkmcnt(0)
	s_barrier
	ds_read_b128 v[100:103], v1
	ds_read_b128 v[104:107], v1 offset:8192
	ds_read_b128 v[108:111], v1 offset:16384
	ds_read_b128 v[112:115], v1 offset:24576
	ds_read_b128 v[116:119], v1 offset:32768
	ds_read_b128 v[120:123], v1 offset:40960
	ds_read_b128 v[124:127], v1 offset:49152
	ds_read_b128 v[128:131], v1 offset:57344
	s_waitcnt lgkmcnt(6)
	v_pk_add_f32 v[12:13], v[102:103], v[106:107]
	v_pk_add_f32 v[246:247], v[100:101], v[104:105]
	s_waitcnt lgkmcnt(5)
	v_pk_add_f32 v[12:13], v[12:13], v[110:111]
	v_pk_add_f32 v[246:247], v[246:247], v[108:109]
	s_waitcnt lgkmcnt(4)
	v_pk_add_f32 v[12:13], v[12:13], v[114:115]
	v_pk_add_f32 v[246:247], v[246:247], v[112:113]
	s_waitcnt lgkmcnt(3)
	v_pk_add_f32 v[12:13], v[12:13], v[118:119]
	v_pk_add_f32 v[246:247], v[246:247], v[116:117]
	s_waitcnt lgkmcnt(2)
	v_pk_add_f32 v[12:13], v[12:13], v[122:123]
	v_pk_add_f32 v[246:247], v[246:247], v[120:121]
	s_waitcnt lgkmcnt(1)
	v_pk_add_f32 v[12:13], v[12:13], v[126:127]
	v_pk_add_f32 v[246:247], v[246:247], v[124:125]
	s_waitcnt lgkmcnt(0)
	v_pk_add_f32 v[12:13], v[12:13], v[130:131]
	v_pk_add_f32 v[246:247], v[246:247], v[128:129]
	s_waitcnt vmcnt(48)
	v_lshlrev_b32_e32 v24, 16, v16
	v_and_b32_e32 v25, 0xffff0000, v16
	v_lshlrev_b32_e32 v26, 16, v14
	v_and_b32_e32 v27, 0xffff0000, v14
	v_pk_mul_f32 v[24:25], v[246:247], v[24:25]
	v_pk_fma_f32 v[22:23], v[198:199], v[26:27], v[24:25]
	v_lshlrev_b32_e32 v24, 16, v17
	v_and_b32_e32 v25, 0xffff0000, v17
	v_lshlrev_b32_e32 v26, 16, v15
	v_and_b32_e32 v27, 0xffff0000, v15
	v_pk_mul_f32 v[24:25], v[12:13], v[24:25]
	v_pk_fma_f32 v[20:21], v[232:233], v[26:27], v[24:25]
	v_cvt_pk_bf16_f32 v14, v22, v23
	v_cvt_pk_bf16_f32 v15, v20, v21
	s_add_i32 s31, s31, s30
	s_add_i32 s0, s0, s1
	s_add_i32 s2, s2, s3
	s_cmpk_lt_i32 s31, 0x100
	global_store_dwordx2 v[10:11], v[14:15], off
	s_cbranch_scc1 .LBB13_853
